# baseline (speedup 1.0000x reference)
_Z14attn_bh_kernelPKDF16_S0_S0_PDF16_i:
	s_load_dwordx4 s[8:11], s[0:1], 0x0
	s_load_dwordx2 s[4:5], s[0:1], 0x10
	s_load_dword s3, s[0:1], 0x20
	v_lshrrev_b32_e32 v2, 6, v0
	v_and_b32_e32 v86, 31, v0
	s_lshr_b32 s6, s2, 3
	s_mul_i32 s12, s6, 0x248
	s_waitcnt lgkmcnt(0)
	v_add_u32_e32 v87, s3, v2
	s_mov_b32 s40, s3
	v_lshl_or_b32 v2, v87, 5, v86
	v_min_i32_e32 v2, 0x247, v2
	v_add_u32_e32 v2, s12, v2
	v_ashrrev_i32_e32 v3, 31, v2
	s_lshl_b32 s3, s2, 6
	v_lshlrev_b64 v[2:3], 10, v[2:3]
	s_and_b32 s14, s3, 0x1c0
	v_bfe_u32 v1, v0, 5, 1
	v_lshl_add_u64 v[2:3], s[8:9], 0, v[2:3]
	s_mov_b32 s7, 0
	s_lshl_b32 s6, s14, 1
	v_mov_b32_e32 v45, 0
	v_lshl_add_u64 v[2:3], v[2:3], 0, s[6:7]
	v_lshlrev_b32_e32 v42, 4, v1
	v_mov_b32_e32 v43, v45
	s_mul_hi_i32 s3, s2, 0x12400
	s_mul_i32 s2, s2, 0x12400
	v_lshl_add_u64 v[2:3], v[2:3], 0, v[42:43]
	s_add_u32 s2, s4, s2
	global_load_dwordx4 v[66:69], v[2:3], off
	global_load_dwordx4 v[70:73], v[2:3], off offset:32
	global_load_dwordx4 v[74:77], v[2:3], off offset:64
	global_load_dwordx4 v[78:81], v[2:3], off offset:96
	s_addc_u32 s3, s5, s3
	s_ashr_i32 s13, s12, 31
	s_lshl_b64 s[16:17], s[12:13], 10
	s_add_u32 s16, s10, s16
	s_addc_u32 s17, s11, s17
	s_add_u32 s16, s16, s6
	s_addc_u32 s17, s17, 0
	v_lshrrev_b32_e32 v4, 6, v0
	v_and_b32_e32 v5, 63, v0
	v_lshrrev_b32_e32 v6, 3, v5
	v_readfirstlane_b32 s15, v4
	v_and_b32_e32 v7, 7, v5
	s_movk_i32 s23, 0x400
	s_movk_i32 s24, 0x490
	s_mov_b32 s19, 0x10000
	s_movk_i32 s20, 0x80
	s_and_b32 s18, s15, 7
	s_lshl_b32 s21, s18, 3
	s_lshl_b32 s18, s18, 10
	v_add_u32_e32 v9, s21, v6
	s_cmp_lt_u32 s15, 8
	s_cselect_b32 s23, s23, s24
	s_cselect_b32 s21, s19, s20
	s_cselect_b32 s16, s16, s2
	s_cselect_b32 s17, s17, s3
	s_cselect_b32 s24, 0, 0x12400
	s_add_u32 s18, s18, s24
	v_bfe_u32 v10, v9, 1, 3
	v_xor_b32_e32 v10, v10, v7
	v_mul_u32_u24_e32 v8, s23, v9
	v_lshl_add_u32 v8, v10, 4, v8
	s_mov_b32 m0, s18
	s_add_u32 s18, s18, 0x2000
	global_load_lds_dwordx4 v8, s[16:17]
	v_add_u32_e32 v8, s21, v8
	s_cmp_lg_u32 s15, 0
	s_cbranch_scc1 .Lat_nw0
	v_add_u32_e32 v11, 0x80000, v8
	s_mov_b32 m0, 0x12000
	s_nop 0
	global_load_lds_dwordx4 v11, s[16:17]

.Lat_nt9:
	v_and_b32_e32 v2, 19, v0
	v_lshlrev_b32_e32 v3, 1, v0
	v_lshrrev_b32_e32 v0, 1, v0
	v_and_b32_e32 v3, 8, v3
	v_and_b32_e32 v0, 4, v0
	v_or3_b32 v0, v3, v2, v0
	v_lshrrev_b32_e32 v2, 1, v0
	v_bfe_u32 v3, v0, 1, 3
	v_lshlrev_b32_e32 v0, 7, v0
	v_bitop3_b32 v2, v1, v2, 7 bitop3:0x78
	v_lshl_add_u32 v88, v2, 4, v0
	v_bitop3_b32 v2, v1, v3, 2 bitop3:0x36
	v_lshl_add_u32 v89, v2, 4, v0
	v_bitop3_b32 v2, v1, v3, 4 bitop3:0x36
	v_lshl_add_u32 v90, v2, 4, v0
	v_bitop3_b32 v2, v1, v3, 6 bitop3:0x36
	v_lshl_add_u32 v91, v2, 4, v0
	v_bfe_u32 v3, v86, 1, 3
	v_lshlrev_b32_e32 v2, 7, v86
	v_add_u32_e32 v2, 0x12400, v2
	v_xor_b32_e32 v4, v1, v3
	v_lshl_add_u32 v93, v4, 4, v2
	v_or_b32_e32 v4, 2, v1
	v_xor_b32_e32 v4, v4, v3
	v_lshl_add_u32 v114, v4, 4, v2
	v_or_b32_e32 v4, 4, v1
	v_xor_b32_e32 v4, v4, v3
	v_lshl_add_u32 v115, v4, 4, v2
	v_or_b32_e32 v4, 6, v1
	v_xor_b32_e32 v4, v4, v3
	v_lshl_add_u32 v116, v4, 4, v2
	s_mov_b32 s22, 1
	s_mov_b32 s33, s15
	v_cmp_gt_i32_e32 vcc, 19, v87
	s_waitcnt lgkmcnt(0)
	s_barrier
	s_mov_b32 m0, s18
	s_add_u32 s18, s18, 0x2000
	global_load_lds_dwordx4 v8, s[16:17]
	v_add_u32_e32 v8, s21, v8
	s_mov_b32 m0, s18
	s_add_u32 s18, s18, 0x2000
	global_load_lds_dwordx4 v8, s[16:17]
	v_add_u32_e32 v8, s21, v8
	s_mov_b32 m0, s18
	s_add_u32 s18, s18, 0x2000
	global_load_lds_dwordx4 v8, s[16:17]
	v_add_u32_e32 v8, s21, v8
	s_mov_b32 m0, s18
	s_add_u32 s18, s18, 0x2000
	global_load_lds_dwordx4 v8, s[16:17]
	v_add_u32_e32 v8, s21, v8
	s_mov_b32 m0, s18
	s_add_u32 s18, s18, 0x2000
	global_load_lds_dwordx4 v8, s[16:17]
	v_add_u32_e32 v8, s21, v8
	s_mov_b32 m0, s18
	s_add_u32 s18, s18, 0x2000
	global_load_lds_dwordx4 v8, s[16:17]
	v_add_u32_e32 v8, s21, v8
	s_mov_b32 m0, s18
	s_add_u32 s18, s18, 0x2000
	global_load_lds_dwordx4 v8, s[16:17]
	v_add_u32_e32 v8, s21, v8
	s_mov_b32 m0, s18
	s_add_u32 s18, s18, 0x2000
	global_load_lds_dwordx4 v8, s[16:17]
	v_add_u32_e32 v8, s21, v8
	s_load_dwordx2 s[4:5], s[0:1], 0x18
	v_lshlrev_b32_e32 v92, 3, v1
	s_add_u32 s0, s8, s6
	v_mov_b32_e32 v0, 0
	s_addc_u32 s1, s9, 0
	v_lshlrev_b32_e32 v2, 1, v92
	v_mov_b32_e32 v3, v0
	v_or_b32_e32 v1, s14, v92
	v_lshl_add_u64 v[82:83], s[0:1], 0, v[2:3]
	s_mov_b32 s7, 0x20000
	s_brev_b32 s6, -2
	s_waitcnt lgkmcnt(0)
	s_and_b32 s5, s5, 0xffff
	s_mov_b64 s[2:3], 0
	s_movk_i32 s13, 0x248
	v_mov_b32_e32 v94, 0x247
	s_movk_i32 s18, 0x205
	s_mov_b32 s19, 0x41000000
	s_mov_b32 s20, 0xc1000000
	v_lshlrev_b32_e32 v95, 1, v1
	v_mov_b32_e32 v96, 0xf149f2ca
	s_mov_b32 s32, 0
	s_mov_b32 s34, 0
	s_cmp_lg_u32 s40, 0
	s_cbranch_scc1 .Lp2_entry
	v_mov_b32_e32 v97, v87
	s_branch .LBB2_9
.LBB2_8:
	s_or_b64 exec, exec, s[8:9]
	s_cmp_lg_u32 s32, 0
	s_cbranch_scc1 .LBB2_31
.Lp2_entry:
	s_cmp_eq_u32 s22, 0
	s_cbranch_scc1 .Lp2_nob
	s_waitcnt vmcnt(0)
	s_barrier
	s_mov_b32 s22, 0
.Lp2_nob:
	s_mov_b32 s32, 1
	s_cmp_ge_u32 s33, 9
	s_cbranch_scc1 .Lp2_idle
	s_mul_i32 s28, s33, 0x5556
	s_lshr_b32 s35, s28, 16
	s_mul_i32 s28, s35, 3
	s_sub_u32 s38, s33, s28
	s_mul_i32 s34, s38, 0xc0
	s_mul_i32 s37, s38, 0x6000
	s_add_u32 s28, s35, 16
	v_mov_b32_e32 v97, s28
	v_mov_b32_e32 v87, -1
	s_branch .LBB2_9

.LBB2_11:
	s_or_b64 exec, exec, s[8:9]
	v_or_b32_e32 v1, 31, v1
	v_min_i32_e32 v2, 0x247, v1
	v_add_u32_e32 v2, 64, v2
	v_ashrrev_i32_e32 v2, 6, v2
	v_cmp_lt_i32_e32 vcc, s18, v1
	v_mov_b32_e32 v17, 0
	v_mov_b32_e32 v35, 0
	v_cndmask_b32_e32 v85, 9, v2, vcc
	v_readfirstlane_b32 s28, v97
	s_cmp_lt_u32 s28, 16
	s_cselect_b32 s29, 1, 0
	s_cmp_eq_u32 s28, 18
	s_cselect_b32 s28, 1, 0
	s_or_b32 s29, s29, s28
	v_subrev_u32_e32 v85, s29, v85
	v_cmp_lt_i32_e32 vcc, 0, v85
	v_mov_b32_e32 v34, 0
	v_mov_b32_e32 v14, 0
	v_mov_b32_e32 v13, 0
	v_mov_b32_e32 v37, 0
	v_mov_b32_e32 v36, 0
	v_mov_b32_e32 v10, 0
	v_mov_b32_e32 v9, 0
	v_mov_b32_e32 v39, 0
	v_mov_b32_e32 v38, 0
	v_mov_b32_e32 v6, 0
	v_mov_b32_e32 v5, 0
	v_mov_b32_e32 v41, 0
	v_mov_b32_e32 v40, 0
	v_mov_b32_e32 v2, 0
	v_mov_b32_e32 v33, 0
	v_mov_b32_e32 v43, 0
	v_mov_b32_e32 v42, 0
	v_mov_b32_e32 v30, 0
	v_mov_b32_e32 v29, 0
	v_mov_b32_e32 v45, 0
	v_mov_b32_e32 v44, 0
	v_mov_b32_e32 v26, 0
	v_mov_b32_e32 v25, 0
	v_mov_b32_e32 v47, 0
	v_mov_b32_e32 v46, 0
	v_mov_b32_e32 v22, 0
	v_mov_b32_e32 v21, 0
	v_mov_b32_e32 v49, 0
	v_mov_b32_e32 v48, 0
	v_mov_b32_e32 v18, 0
	v_mov_b32_e32 v1, 0
	s_and_saveexec_b64 s[8:9], vcc
	s_cbranch_execz .LBB2_23
	v_mov_b32_e32 v14, v0
	v_mov_b32_e32 v15, v0
	v_max_i32_e32 v98, 0x205, v3
	v_mov_b32_e32 v1, v0
	v_mov_b32_e32 v2, v0
	v_mov_b32_e32 v3, v0
	v_mov_b32_e32 v4, v0
	v_mov_b32_e32 v5, v0
	v_mov_b32_e32 v6, v0
	v_mov_b32_e32 v7, v0
	v_mov_b32_e32 v8, v0
	v_mov_b32_e32 v9, v0
	v_mov_b32_e32 v10, v0
	v_mov_b32_e32 v11, v0
	v_mov_b32_e32 v12, v0
	v_mov_b32_e32 v13, v0
	v_mov_b64_e32 v[32:33], v[14:15]
	v_mov_b64_e32 v[30:31], v[12:13]
	v_mov_b64_e32 v[28:29], v[10:11]
	v_mov_b64_e32 v[26:27], v[8:9]
	v_mov_b64_e32 v[24:25], v[6:7]
	v_mov_b64_e32 v[22:23], v[4:5]
	v_mov_b64_e32 v[20:21], v[2:3]
	v_mov_b64_e32 v[18:19], v[0:1]
	v_mov_b64_e32 v[16:17], v[14:15]
	s_mov_b32 s21, 0
	v_mov_b32_e32 v104, 0
	s_mov_b32 s31, 0
	s_mov_b64 s[10:11], 0
	v_mov_b64_e32 v[14:15], v[12:13]
	v_mov_b64_e32 v[12:13], v[10:11]
	v_mov_b64_e32 v[10:11], v[8:9]
	v_mov_b64_e32 v[8:9], v[6:7]
	v_mov_b64_e32 v[6:7], v[4:5]
	v_mov_b64_e32 v[4:5], v[2:3]
	v_mov_b64_e32 v[2:3], v[0:1]
	v_mov_b32_e32 v1, 0
	v_mov_b32_e32 v99, v88
	v_mov_b32_e32 v100, v89
	v_mov_b32_e32 v101, v90
	v_mov_b32_e32 v102, v91
	v_mov_b32_e32 v103, v93
	v_readfirstlane_b32 s30, v85
	v_mov_b32_e32 v117, v114
	v_mov_b32_e32 v118, v115
	v_mov_b32_e32 v119, v116
	s_cmp_eq_u32 s32, 0
	s_cbranch_scc1 .Lp_rng1
	s_mov_b32 s30, 3
	s_cmp_eq_u32 s38, 2
	s_cselect_b32 s39, 1, 0
	s_and_b32 s29, s29, s39
	s_mov_b32 s21, s34
	v_add_u32_e32 v99, s37, v99
	v_add_u32_e32 v100, s37, v100
	v_add_u32_e32 v101, s37, v101
	v_add_u32_e32 v102, s37, v102
	v_add_u32_e32 v103, s37, v103
	v_add_u32_e32 v117, s37, v117
	v_add_u32_e32 v118, s37, v118
	v_add_u32_e32 v119, s37, v119
.Lp_rng1:
	s_branch .LBB2_14
.LBB2_13:
	v_exp_f32_e32 v105, v50
	v_exp_f32_e32 v106, v51
	v_exp_f32_e32 v107, v52
	v_exp_f32_e32 v108, v53
	ds_read_b128 v[50:53], v103
	v_exp_f32_e32 v109, v54
	v_exp_f32_e32 v110, v55
	v_exp_f32_e32 v111, v56
	v_exp_f32_e32 v57, v57
	v_cvt_pkrtz_f16_f32 v54, v105, v106
	v_cvt_pkrtz_f16_f32 v55, v107, v108
	v_cvt_pkrtz_f16_f32 v56, v109, v110
	v_cvt_pkrtz_f16_f32 v57, v111, v57
	ds_read_b128 v[106:109], v117
	v_exp_f32_e32 v105, v58
	s_waitcnt lgkmcnt(1)
	v_mfma_f32_32x32x16_f16 v[18:33], v[50:53], v[54:57], v[18:33]
	ds_read_b128 v[50:53], v103 offset:4096
	v_exp_f32_e32 v110, v59
	v_exp_f32_e32 v111, v60
	v_exp_f32_e32 v112, v61
	ds_read_b128 v[58:61], v117 offset:4096
	v_exp_f32_e32 v62, v62
	v_exp_f32_e32 v41, v41
	s_waitcnt lgkmcnt(1)
	v_mfma_f32_32x32x16_f16 v[2:17], v[50:53], v[54:57], v[2:17]
	v_exp_f32_e32 v52, v63
	v_exp_f32_e32 v53, v64
	v_exp_f32_e32 v63, v65
	v_cvt_pkrtz_f16_f32 v50, v105, v110
	v_cvt_pkrtz_f16_f32 v51, v111, v112
	v_cvt_pkrtz_f16_f32 v52, v62, v52
	v_cvt_pkrtz_f16_f32 v53, v53, v63
	v_exp_f32_e32 v62, v34
	v_exp_f32_e32 v63, v35
	v_exp_f32_e32 v64, v36
	v_exp_f32_e32 v65, v37
	ds_read_b128 v[34:37], v118
	v_mfma_f32_32x32x16_f16 v[18:33], v[106:109], v[50:53], v[18:33]
	v_exp_f32_e32 v105, v38
	v_exp_f32_e32 v106, v39
	v_cvt_pkrtz_f16_f32 v38, v62, v63
	v_cvt_pkrtz_f16_f32 v39, v64, v65
	v_exp_f32_e32 v62, v42
	v_exp_f32_e32 v63, v43
	v_exp_f32_e32 v64, v44
	s_waitcnt lgkmcnt(1)
	v_mfma_f32_32x32x16_f16 v[2:17], v[58:61], v[50:53], v[2:17]
	v_exp_f32_e32 v58, v40
	v_cvt_pkrtz_f16_f32 v40, v105, v106
	v_exp_f32_e32 v65, v45
	ds_read_b128 v[42:45], v119 offset:4096
	v_cvt_pkrtz_f16_f32 v41, v58, v41
	ds_read_b128 v[58:61], v119
	v_exp_f32_e32 v46, v46
	s_waitcnt lgkmcnt(2)
	v_mfma_f32_32x32x16_f16 v[18:33], v[34:37], v[38:41], v[18:33]
	ds_read_b128 v[34:37], v118 offset:4096
	s_add_i32 s21, s21, 64
	v_add_u32_e32 v99, 0x2000, v99
	v_add_u32_e32 v100, 0x2000, v100
	v_add_u32_e32 v101, 0x2000, v101
	s_waitcnt lgkmcnt(0)
	v_mfma_f32_32x32x16_f16 v[2:17], v[34:37], v[38:41], v[2:17]
	v_exp_f32_e32 v36, v47
	v_exp_f32_e32 v37, v48
	v_exp_f32_e32 v47, v49
	v_cvt_pkrtz_f16_f32 v34, v62, v63
	v_cvt_pkrtz_f16_f32 v35, v64, v65
	v_cvt_pkrtz_f16_f32 v36, v46, v36
	v_cvt_pkrtz_f16_f32 v37, v37, v47
	v_pk_add_f16 v46, v55, v51
	v_pk_add_f16 v47, v57, v53
	v_pk_add_f16 v48, v54, v50
	v_pk_add_f16 v49, v56, v52
	v_pk_add_f16 v39, v39, v35
	v_pk_add_f16 v41, v41, v37
	v_pk_add_f16 v38, v38, v34
	v_pk_add_f16 v40, v40, v36
	v_pk_add_f16 v38, v38, v48
	v_pk_add_f16 v40, v40, v49
	v_pk_add_f16 v41, v41, v47
	v_pk_add_f16 v39, v39, v46
	v_mfma_f32_32x32x16_f16 v[18:33], v[58:61], v[34:37], v[18:33]
	v_pk_add_f16 v39, v39, v41
	v_pk_add_f16 v38, v38, v40
	v_add_u32_e32 v102, 0x2000, v102
	v_mfma_f32_32x32x16_f16 v[2:17], v[42:45], v[34:37], v[2:17]
	v_fma_mix_f32 v1, v39, 1.0, v1 op_sel_hi:[1,0,0]
	v_fma_mix_f32 v1, v39, 1.0, v1 op_sel:[1,0,0] op_sel_hi:[1,0,0]
	v_fma_mix_f32 v1, v38, 1.0, v1 op_sel_hi:[1,0,0]
	v_fma_mix_f32 v1, v38, 1.0, v1 op_sel:[1,0,0] op_sel_hi:[1,0,0]
	s_add_i32 s30, s30, -1
	v_add_u32_e32 v103, 0x2000, v103
	v_add_u32_e32 v117, 0x2000, v117
	v_add_u32_e32 v118, 0x2000, v118
	v_add_u32_e32 v119, 0x2000, v119
	s_cmp_eq_u32 s30, 0
	s_cbranch_scc1 .LBB2_22

.LBB2_16:
	s_nop 9
	v_max_f32_e32 v105, v50, v51
	v_max3_f32 v106, v34, v35, v36
	v_max3_f32 v105, v105, v52, v53
	v_max3_f32 v105, v105, v37, v54
	v_max3_f32 v106, v106, v38, v39
	v_max3_f32 v105, v105, v55, v56
	v_max3_f32 v106, v106, v40, v41
	v_max3_f32 v105, v105, v57, v58
	v_max3_f32 v106, v106, v42, v43
	v_max3_f32 v105, v105, v59, v60
	v_max3_f32 v106, v106, v44, v45
	v_max3_f32 v105, v105, v61, v62
	v_max3_f32 v106, v106, v46, v47
	v_max3_f32 v105, v105, v63, v64
	v_max3_f32 v106, v106, v48, v49
	v_max3_f32 v105, v105, v65, v106
	v_mov_b32_e32 v106, v105
	s_nop 1
	v_permlane32_swap_b32_e32 v105, v106
	v_max_f32_e32 v105, v105, v106
	v_sub_f32_e32 v106, v105, v104
	v_cmp_lt_f32_e32 vcc, s19, v106
	s_cmp_lg_u32 s21, s34
	s_cbranch_scc1 .Lat_thr
	v_cmp_gt_f32_e64 s[16:17], s20, v105
	s_or_b64 vcc, vcc, s[16:17]

.Lat_exit:
	s_cmp_lg_u32 s32, 0
	s_cbranch_scc1 .Lp2_after

.Lp2_after:
	s_barrier
	s_cmp_eq_u32 s38, 0
	s_cbranch_scc1 .Lp2_b4
	v_mbcnt_lo_u32_b32 v105, -1, 0
	v_mbcnt_hi_u32_b32 v105, -1, v105
	s_mul_i32 s36, s33, 0x2200
	v_lshlrev_b32_e32 v106, 3, v105
	v_lshlrev_b32_e32 v105, 4, v105
	v_add_u32_e32 v105, s36, v105
	v_add_u32_e32 v106, s36, v106
	ds_write_b128 v105, v[2:5]
	ds_write_b128 v105, v[6:9] offset:1024
	ds_write_b128 v105, v[10:13] offset:2048
	ds_write_b128 v105, v[14:17] offset:3072
	ds_write_b128 v105, v[18:21] offset:4096
	ds_write_b128 v105, v[22:25] offset:5120
	ds_write_b128 v105, v[26:29] offset:6144
	ds_write_b128 v105, v[30:33] offset:7168
	v_mov_b32_e32 v108, v1
	v_mov_b32_e32 v109, v104
	ds_write_b64 v106, v[108:109] offset:8192
	s_waitcnt lgkmcnt(0)
.Lp2_b4:
	s_barrier
	s_cmp_lg_u32 s38, 0
	s_cbranch_scc1 .LBB2_31
	v_mbcnt_lo_u32_b32 v105, -1, 0
	v_mbcnt_hi_u32_b32 v105, -1, v105
	s_mul_i32 s36, s33, 0x2200
	s_add_u32 s36, s36, 0x2200
	v_lshlrev_b32_e32 v106, 3, v105
	v_lshlrev_b32_e32 v105, 4, v105
	v_add_u32_e32 v105, s36, v105
	v_add_u32_e32 v106, s36, v106
	ds_read_b64 v[108:109], v106 offset:8192
	ds_read_b64 v[110:111], v106 offset:16896
	ds_read_b128 v[34:37], v105
	ds_read_b128 v[38:41], v105 offset:1024
	ds_read_b128 v[42:45], v105 offset:2048
	ds_read_b128 v[46:49], v105 offset:3072
	ds_read_b128 v[50:53], v105 offset:4096
	ds_read_b128 v[54:57], v105 offset:5120
	ds_read_b128 v[58:61], v105 offset:6144
	ds_read_b128 v[62:65], v105 offset:7168
	s_waitcnt lgkmcnt(8)
	v_max3_f32 v112, v104, v109, v111
	v_sub_f32_e32 v113, v104, v112
	v_exp_f32_e32 v113, v113
	v_sub_f32_e32 v109, v109, v112
	v_exp_f32_e32 v109, v109
	v_sub_f32_e32 v111, v111, v112
	v_exp_f32_e32 v111, v111
	s_nop 0
	v_mul_f32_e32 v1, v1, v113
	v_fmac_f32_e32 v1, v108, v109
	v_fmac_f32_e32 v1, v110, v111
	v_mul_f32_e32 v2, v2, v113
	v_mul_f32_e32 v3, v3, v113
	v_mul_f32_e32 v4, v4, v113
	v_mul_f32_e32 v5, v5, v113
	v_mul_f32_e32 v6, v6, v113
	v_mul_f32_e32 v7, v7, v113
	v_mul_f32_e32 v8, v8, v113
	v_mul_f32_e32 v9, v9, v113
	v_mul_f32_e32 v10, v10, v113
	v_mul_f32_e32 v11, v11, v113
	v_mul_f32_e32 v12, v12, v113
	v_mul_f32_e32 v13, v13, v113
	v_mul_f32_e32 v14, v14, v113
	v_mul_f32_e32 v15, v15, v113
	v_mul_f32_e32 v16, v16, v113
	v_mul_f32_e32 v17, v17, v113
	v_mul_f32_e32 v18, v18, v113
	v_mul_f32_e32 v19, v19, v113
	v_mul_f32_e32 v20, v20, v113
	v_mul_f32_e32 v21, v21, v113
	v_mul_f32_e32 v22, v22, v113
	v_mul_f32_e32 v23, v23, v113
	v_mul_f32_e32 v24, v24, v113
	v_mul_f32_e32 v25, v25, v113
	v_mul_f32_e32 v26, v26, v113
	v_mul_f32_e32 v27, v27, v113
	v_mul_f32_e32 v28, v28, v113
	v_mul_f32_e32 v29, v29, v113
	v_mul_f32_e32 v30, v30, v113
	v_mul_f32_e32 v31, v31, v113
	v_mul_f32_e32 v32, v32, v113
	v_mul_f32_e32 v33, v33, v113
	s_waitcnt lgkmcnt(0)
	v_fmac_f32_e32 v2, v109, v34
	v_fmac_f32_e32 v3, v109, v35
	v_fmac_f32_e32 v4, v109, v36
	v_fmac_f32_e32 v5, v109, v37
	v_fmac_f32_e32 v6, v109, v38
	v_fmac_f32_e32 v7, v109, v39
	v_fmac_f32_e32 v8, v109, v40
	v_fmac_f32_e32 v9, v109, v41
	v_fmac_f32_e32 v10, v109, v42
	v_fmac_f32_e32 v11, v109, v43
	v_fmac_f32_e32 v12, v109, v44
	v_fmac_f32_e32 v13, v109, v45
	v_fmac_f32_e32 v14, v109, v46
	v_fmac_f32_e32 v15, v109, v47
	v_fmac_f32_e32 v16, v109, v48
	v_fmac_f32_e32 v17, v109, v49
	v_fmac_f32_e32 v18, v109, v50
	v_fmac_f32_e32 v19, v109, v51
	v_fmac_f32_e32 v20, v109, v52
	v_fmac_f32_e32 v21, v109, v53
	v_fmac_f32_e32 v22, v109, v54
	v_fmac_f32_e32 v23, v109, v55
	v_fmac_f32_e32 v24, v109, v56
	v_fmac_f32_e32 v25, v109, v57
	v_fmac_f32_e32 v26, v109, v58
	v_fmac_f32_e32 v27, v109, v59
	v_fmac_f32_e32 v28, v109, v60
	v_fmac_f32_e32 v29, v109, v61
	v_fmac_f32_e32 v30, v109, v62
	v_fmac_f32_e32 v31, v109, v63
	v_fmac_f32_e32 v32, v109, v64
	v_fmac_f32_e32 v33, v109, v65
	ds_read_b128 v[34:37], v105 offset:8704
	ds_read_b128 v[38:41], v105 offset:9728
	ds_read_b128 v[42:45], v105 offset:10752
	ds_read_b128 v[46:49], v105 offset:11776
	ds_read_b128 v[50:53], v105 offset:12800
	ds_read_b128 v[54:57], v105 offset:13824
	ds_read_b128 v[58:61], v105 offset:14848
	ds_read_b128 v[62:65], v105 offset:15872
	s_waitcnt lgkmcnt(0)
	v_fmac_f32_e32 v2, v111, v34
	v_fmac_f32_e32 v3, v111, v35
	v_fmac_f32_e32 v4, v111, v36
	v_fmac_f32_e32 v5, v111, v37
	v_fmac_f32_e32 v6, v111, v38
	v_fmac_f32_e32 v7, v111, v39
	v_fmac_f32_e32 v8, v111, v40
	v_fmac_f32_e32 v9, v111, v41
	v_fmac_f32_e32 v10, v111, v42
	v_fmac_f32_e32 v11, v111, v43
	v_fmac_f32_e32 v12, v111, v44
	v_fmac_f32_e32 v13, v111, v45
	v_fmac_f32_e32 v14, v111, v46
	v_fmac_f32_e32 v15, v111, v47
	v_fmac_f32_e32 v16, v111, v48
	v_fmac_f32_e32 v17, v111, v49
	v_fmac_f32_e32 v18, v111, v50
	v_fmac_f32_e32 v19, v111, v51
	v_fmac_f32_e32 v20, v111, v52
	v_fmac_f32_e32 v21, v111, v53
	v_fmac_f32_e32 v22, v111, v54
	v_fmac_f32_e32 v23, v111, v55
	v_fmac_f32_e32 v24, v111, v56
	v_fmac_f32_e32 v25, v111, v57
	v_fmac_f32_e32 v26, v111, v58
	v_fmac_f32_e32 v27, v111, v59
	v_fmac_f32_e32 v28, v111, v60
	v_fmac_f32_e32 v29, v111, v61
	v_fmac_f32_e32 v30, v111, v62
	v_fmac_f32_e32 v31, v111, v63
	v_fmac_f32_e32 v32, v111, v64
	v_fmac_f32_e32 v33, v111, v65
	s_branch .Lat_epi
.Lp2_idle:
	s_barrier
	s_barrier
	s_branch .LBB2_31
	.p2align	8

	.amdhsa_kernel _Z14attn_bh_kernelPKDF16_S0_S0_PDF16_i
		.amdhsa_group_segment_fixed_size 0
		.amdhsa_private_segment_fixed_size 0
		.amdhsa_kernarg_size 36
		.amdhsa_user_sgpr_count 2
		.amdhsa_user_sgpr_dispatch_ptr 0
		.amdhsa_user_sgpr_queue_ptr 0
		.amdhsa_user_sgpr_kernarg_segment_ptr 1
		.amdhsa_user_sgpr_dispatch_id 0
		.amdhsa_user_sgpr_kernarg_preload_length 0
		.amdhsa_user_sgpr_kernarg_preload_offset 0
		.amdhsa_user_sgpr_private_segment_size 0
		.amdhsa_uses_dynamic_stack 0
		.amdhsa_enable_private_segment 0
		.amdhsa_system_sgpr_workgroup_id_x 1
		.amdhsa_system_sgpr_workgroup_id_y 0
		.amdhsa_system_sgpr_workgroup_id_z 0
		.amdhsa_system_sgpr_workgroup_info 0
		.amdhsa_system_vgpr_workitem_id 0
		.amdhsa_next_free_vgpr 120
		.amdhsa_next_free_sgpr 41
		.amdhsa_accum_offset 120
		.amdhsa_reserve_vcc 1
		.amdhsa_float_round_mode_32 0
		.amdhsa_float_round_mode_16_64 0
		.amdhsa_float_denorm_mode_32 3
		.amdhsa_float_denorm_mode_16_64 3
		.amdhsa_dx10_clamp 1
		.amdhsa_ieee_mode 1
		.amdhsa_fp16_overflow 0
		.amdhsa_tg_split 0
		.amdhsa_exception_fp_ieee_invalid_op 0
		.amdhsa_exception_fp_denorm_src 0
		.amdhsa_exception_fp_ieee_div_zero 0
		.amdhsa_exception_fp_ieee_overflow 0
		.amdhsa_exception_fp_ieee_underflow 0
		.amdhsa_exception_fp_ieee_inexact 0
		.amdhsa_exception_int_div_zero 0
	.end_amdhsa_kernel

amdhsa.kernels:
  - .agpr_count:     0
    .args:
      - .offset:         0
        .size:           136
        .value_kind:     by_value
      - .actual_access:  read_only
        .address_space:  global
        .offset:         136
        .size:           8
        .value_kind:     global_buffer
      - .actual_access:  read_only
        .address_space:  global
        .offset:         144
        .size:           8
        .value_kind:     global_buffer
      - .actual_access:  read_only
        .address_space:  global
        .offset:         152
        .size:           8
        .value_kind:     global_buffer
      - .actual_access:  read_only
        .address_space:  global
        .offset:         160
        .size:           8
        .value_kind:     global_buffer
      - .actual_access:  write_only
        .address_space:  global
        .offset:         168
        .size:           8
        .value_kind:     global_buffer
      - .actual_access:  write_only
        .address_space:  global
        .offset:         176
        .size:           8
        .value_kind:     global_buffer
    .group_segment_fixed_size: 0
    .kernarg_segment_align: 8
    .kernarg_segment_size: 184
    .language:       OpenCL C
    .language_version:
      - 2
      - 0
    .max_flat_workgroup_size: 256
    .name:           _Z15prologue_kernel8PrepArgsPKfS1_PKiS1_PDF16_Pf
    .private_segment_fixed_size: 0
    .sgpr_count:     36
    .sgpr_spill_count: 0
    .symbol:         _Z15prologue_kernel8PrepArgsPKfS1_PKiS1_PDF16_Pf.kd
    .uniform_work_group_size: 1
    .uses_dynamic_stack: false
    .vgpr_count:     44
    .vgpr_spill_count: 0
    .wavefront_size: 64
  - .agpr_count:     0
    .args:
      - .actual_access:  read_only
        .address_space:  global
        .offset:         0
        .size:           8
        .value_kind:     global_buffer
      - .offset:         8
        .size:           4
        .value_kind:     by_value
      - .offset:         12
        .size:           4
        .value_kind:     by_value
      - .actual_access:  read_only
        .address_space:  global
        .offset:         16
        .size:           8
        .value_kind:     global_buffer
      - .actual_access:  read_only
        .address_space:  global
        .offset:         24
        .size:           8
        .value_kind:     global_buffer
      - .actual_access:  read_only
        .address_space:  global
        .offset:         32
        .size:           8
        .value_kind:     global_buffer
      - .actual_access:  read_only
        .address_space:  global
        .offset:         40
        .size:           8
        .value_kind:     global_buffer
      - .address_space:  global
        .offset:         48
        .size:           8
        .value_kind:     global_buffer
      - .actual_access:  write_only
        .address_space:  global
        .offset:         56
        .size:           8
        .value_kind:     global_buffer
    .group_segment_fixed_size: 0
    .kernarg_segment_align: 8
    .kernarg_segment_size: 64
    .language:       OpenCL C
    .language_version:
      - 2
      - 0
    .max_flat_workgroup_size: 256
    .name:           _Z18ffn2_finish_kernelPKfiiS0_PK15HIP_vector_typeIfLj2EES0_S0_PDF16_PS2_
    .private_segment_fixed_size: 0
    .sgpr_count:     20
    .sgpr_spill_count: 0
    .symbol:         _Z18ffn2_finish_kernelPKfiiS0_PK15HIP_vector_typeIfLj2EES0_S0_PDF16_PS2_.kd
    .uniform_work_group_size: 1
    .uses_dynamic_stack: false
    .vgpr_count:     52
    .vgpr_spill_count: 0
    .wavefront_size: 64
  - .agpr_count:     0
    .args:
      - .actual_access:  read_only
        .address_space:  global
        .offset:         0
        .size:           8
        .value_kind:     global_buffer
      - .actual_access:  read_only
        .address_space:  global
        .offset:         8
        .size:           8
        .value_kind:     global_buffer
      - .actual_access:  read_only
        .address_space:  global
        .offset:         16
        .size:           8
        .value_kind:     global_buffer
      - .actual_access:  write_only
        .address_space:  global
        .offset:         24
        .size:           8
        .value_kind:     global_buffer
      - .offset:         32
        .size:           4
        .value_kind:     by_value
    .group_segment_fixed_size: 0
    .kernarg_segment_align: 8
    .kernarg_segment_size: 36
    .language:       OpenCL C
    .language_version:
      - 2
      - 0
    .max_flat_workgroup_size: 1024
    .name:           _Z14attn_bh_kernelPKDF16_S0_S0_PDF16_i
    .private_segment_fixed_size: 0
    .sgpr_count:     47
    .sgpr_spill_count: 0
    .symbol:         _Z14attn_bh_kernelPKDF16_S0_S0_PDF16_i.kd
    .uniform_work_group_size: 1
    .uses_dynamic_stack: false
    .vgpr_count:     120
    .vgpr_spill_count: 0
    .wavefront_size: 64
  - .agpr_count:     0
    .args:
      - .offset:         0
        .size:           336
        .value_kind:     by_value
    .group_segment_fixed_size: 0
    .kernarg_segment_align: 8
    .kernarg_segment_size: 336
    .language:       OpenCL C
    .language_version:
      - 2
      - 0
    .max_flat_workgroup_size: 256
    .name:           _Z11gemm_kernelILi0EEv8GemmArgs
    .private_segment_fixed_size: 0
    .sgpr_count:     47
    .sgpr_spill_count: 0
    .symbol:         _Z11gemm_kernelILi0EEv8GemmArgs.kd
    .uniform_work_group_size: 1
    .uses_dynamic_stack: false
    .vgpr_count:     198
    .vgpr_spill_count: 0
    .wavefront_size: 64
  - .agpr_count:     0
    .args:
      - .offset:         0
        .size:           336
        .value_kind:     by_value
    .group_segment_fixed_size: 0
    .kernarg_segment_align: 8
    .kernarg_segment_size: 336
    .language:       OpenCL C
    .language_version:
      - 2
      - 0
    .max_flat_workgroup_size: 256
    .name:           _Z11gemm_kernelILi1EEv8GemmArgs
    .private_segment_fixed_size: 0
    .sgpr_count:     43
    .sgpr_spill_count: 0
    .symbol:         _Z11gemm_kernelILi1EEv8GemmArgs.kd
    .uniform_work_group_size: 1
    .uses_dynamic_stack: false
    .vgpr_count:     202
    .vgpr_spill_count: 0
    .wavefront_size: 64
  - .agpr_count:     0
    .args:
      - .offset:         0
        .size:           336
        .value_kind:     by_value
    .group_segment_fixed_size: 0
    .kernarg_segment_align: 8
    .kernarg_segment_size: 336
    .language:       OpenCL C
    .language_version:
      - 2
      - 0
    .max_flat_workgroup_size: 256
    .name:           _Z11gemm_kernelILi2EEv8GemmArgs
    .private_segment_fixed_size: 0
    .sgpr_count:     41
    .sgpr_spill_count: 0
    .symbol:         _Z11gemm_kernelILi2EEv8GemmArgs.kd
    .uniform_work_group_size: 1
    .uses_dynamic_stack: false
    .vgpr_count:     198
    .vgpr_spill_count: 0
    .wavefront_size: 64
  - .agpr_count:     0
    .args:
      - .offset:         0
        .size:           336
        .value_kind:     by_value
      - .offset:         336
        .size:           4
        .value_kind:     hidden_block_count_x
      - .offset:         340
        .size:           4
        .value_kind:     hidden_block_count_y
      - .offset:         344
        .size:           4
        .value_kind:     hidden_block_count_z
      - .offset:         348
        .size:           2
        .value_kind:     hidden_group_size_x
      - .offset:         350
        .size:           2
        .value_kind:     hidden_group_size_y
      - .offset:         352
        .size:           2
        .value_kind:     hidden_group_size_z
      - .offset:         354
        .size:           2
        .value_kind:     hidden_remainder_x
      - .offset:         356
        .size:           2
        .value_kind:     hidden_remainder_y
      - .offset:         358
        .size:           2
        .value_kind:     hidden_remainder_z
      - .offset:         376
        .size:           8
        .value_kind:     hidden_global_offset_x
      - .offset:         384
        .size:           8
        .value_kind:     hidden_global_offset_y
      - .offset:         392
        .size:           8
        .value_kind:     hidden_global_offset_z
      - .offset:         400
        .size:           2
        .value_kind:     hidden_grid_dims
      - .offset:         456
        .size:           4
        .value_kind:     hidden_dynamic_lds_size
    .group_segment_fixed_size: 0
    .kernarg_segment_align: 8
    .kernarg_segment_size: 592
    .language:       OpenCL C
    .language_version:
      - 2
      - 0
    .max_flat_workgroup_size: 512
    .name:           _Z14gemm256_kernelILi0ELi512ELi1536EEv8GemmArgs
    .private_segment_fixed_size: 0
    .sgpr_count:     78
    .sgpr_spill_count: 0
    .symbol:         _Z14gemm256_kernelILi0ELi512ELi1536EEv8GemmArgs.kd
    .uniform_work_group_size: 1
    .uses_dynamic_stack: false
    .vgpr_count:     256
    .vgpr_spill_count: 0
    .wavefront_size: 64
  - .agpr_count:     0
    .args:
      - .offset:         0
        .size:           336
        .value_kind:     by_value
      - .offset:         336
        .size:           4
        .value_kind:     hidden_block_count_x
      - .offset:         340
        .size:           4
        .value_kind:     hidden_block_count_y
      - .offset:         344
        .size:           4
        .value_kind:     hidden_block_count_z
      - .offset:         348
        .size:           2
        .value_kind:     hidden_group_size_x
      - .offset:         350
        .size:           2
        .value_kind:     hidden_group_size_y
      - .offset:         352
        .size:           2
        .value_kind:     hidden_group_size_z
      - .offset:         354
        .size:           2
        .value_kind:     hidden_remainder_x
      - .offset:         356
        .size:           2
        .value_kind:     hidden_remainder_y
      - .offset:         358
        .size:           2
        .value_kind:     hidden_remainder_z
      - .offset:         376
        .size:           8
        .value_kind:     hidden_global_offset_x
      - .offset:         384
        .size:           8
        .value_kind:     hidden_global_offset_y
      - .offset:         392
        .size:           8
        .value_kind:     hidden_global_offset_z
      - .offset:         400
        .size:           2
        .value_kind:     hidden_grid_dims
      - .offset:         456
        .size:           4
        .value_kind:     hidden_dynamic_lds_size
    .group_segment_fixed_size: 0
    .kernarg_segment_align: 8
    .kernarg_segment_size: 592
    .language:       OpenCL C
    .language_version:
      - 2
      - 0
    .max_flat_workgroup_size: 512
    .name:           _Z14gemm256_kernelILi0ELi512ELi1024EEv8GemmArgs
    .private_segment_fixed_size: 0
    .sgpr_count:     78
    .sgpr_spill_count: 0
    .symbol:         _Z14gemm256_kernelILi0ELi512ELi1024EEv8GemmArgs.kd
    .uniform_work_group_size: 1
    .uses_dynamic_stack: false
    .vgpr_count:     256
    .vgpr_spill_count: 0
    .wavefront_size: 64
  - .agpr_count:     0
    .args:
      - .offset:         0
        .size:           336
        .value_kind:     by_value
      - .offset:         336
        .size:           4
        .value_kind:     hidden_block_count_x
      - .offset:         340
        .size:           4
        .value_kind:     hidden_block_count_y
      - .offset:         344
        .size:           4
        .value_kind:     hidden_block_count_z
      - .offset:         348
        .size:           2
        .value_kind:     hidden_group_size_x
      - .offset:         350
        .size:           2
        .value_kind:     hidden_group_size_y
      - .offset:         352
        .size:           2
        .value_kind:     hidden_group_size_z
      - .offset:         354
        .size:           2
        .value_kind:     hidden_remainder_x
      - .offset:         356
        .size:           2
        .value_kind:     hidden_remainder_y
      - .offset:         358
        .size:           2
        .value_kind:     hidden_remainder_z
      - .offset:         376
        .size:           8
        .value_kind:     hidden_global_offset_x
      - .offset:         384
        .size:           8
        .value_kind:     hidden_global_offset_y
      - .offset:         392
        .size:           8
        .value_kind:     hidden_global_offset_z
      - .offset:         400
        .size:           2
        .value_kind:     hidden_grid_dims
      - .offset:         456
        .size:           4
        .value_kind:     hidden_dynamic_lds_size
    .group_segment_fixed_size: 0
    .kernarg_segment_align: 8
    .kernarg_segment_size: 592
    .language:       OpenCL C
    .language_version:
      - 2
      - 0
    .max_flat_workgroup_size: 512
    .name:           _Z14gemm256_kernelILi1ELi512ELi512EEv8GemmArgs
    .private_segment_fixed_size: 0
    .sgpr_count:     81
    .sgpr_spill_count: 0
    .symbol:         _Z14gemm256_kernelILi1ELi512ELi512EEv8GemmArgs.kd
    .uniform_work_group_size: 1
    .uses_dynamic_stack: false
    .vgpr_count:     256
    .vgpr_spill_count: 0
    .wavefront_size: 64
  - .agpr_count:     0
    .args:
      - .offset:         0
        .size:           336
        .value_kind:     by_value
      - .offset:         336
        .size:           4
        .value_kind:     hidden_block_count_x
      - .offset:         340
        .size:           4
        .value_kind:     hidden_block_count_y
      - .offset:         344
        .size:           4
        .value_kind:     hidden_block_count_z
      - .offset:         348
        .size:           2
        .value_kind:     hidden_group_size_x
      - .offset:         350
        .size:           2
        .value_kind:     hidden_group_size_y
      - .offset:         352
        .size:           2
        .value_kind:     hidden_group_size_z
      - .offset:         354
        .size:           2
        .value_kind:     hidden_remainder_x
      - .offset:         356
        .size:           2
        .value_kind:     hidden_remainder_y
      - .offset:         358
        .size:           2
        .value_kind:     hidden_remainder_z
      - .offset:         376
        .size:           8
        .value_kind:     hidden_global_offset_x
      - .offset:         384
        .size:           8
        .value_kind:     hidden_global_offset_y
      - .offset:         392
        .size:           8
        .value_kind:     hidden_global_offset_z
      - .offset:         400
        .size:           2
        .value_kind:     hidden_grid_dims
      - .offset:         456
        .size:           4
        .value_kind:     hidden_dynamic_lds_size
    .group_segment_fixed_size: 0
    .kernarg_segment_align: 8
    .kernarg_segment_size: 592
    .language:       OpenCL C
    .language_version:
      - 2
      - 0
    .max_flat_workgroup_size: 512
    .name:           _Z14gemm256_kernelILi2ELi512ELi2048EEv8GemmArgs
    .private_segment_fixed_size: 0
    .sgpr_count:     68
    .sgpr_spill_count: 0
    .symbol:         _Z14gemm256_kernelILi2ELi512ELi2048EEv8GemmArgs.kd
    .uniform_work_group_size: 1
    .uses_dynamic_stack: false
    .vgpr_count:     254
    .vgpr_spill_count: 0
    .wavefront_size: 64
  - .agpr_count:     0
    .args:
      - .offset:         0
        .size:           336
        .value_kind:     by_value
      - .offset:         336
        .size:           4
        .value_kind:     hidden_block_count_x
      - .offset:         340
        .size:           4
        .value_kind:     hidden_block_count_y
      - .offset:         344
        .size:           4
        .value_kind:     hidden_block_count_z
      - .offset:         348
        .size:           2
        .value_kind:     hidden_group_size_x
      - .offset:         350
        .size:           2
        .value_kind:     hidden_group_size_y
      - .offset:         352
        .size:           2
        .value_kind:     hidden_group_size_z
      - .offset:         354
        .size:           2
        .value_kind:     hidden_remainder_x
      - .offset:         356
        .size:           2
        .value_kind:     hidden_remainder_y
      - .offset:         358
        .size:           2
        .value_kind:     hidden_remainder_z
      - .offset:         376
        .size:           8
        .value_kind:     hidden_global_offset_x
      - .offset:         384
        .size:           8
        .value_kind:     hidden_global_offset_y
      - .offset:         392
        .size:           8
        .value_kind:     hidden_global_offset_z
      - .offset:         400
        .size:           2
        .value_kind:     hidden_grid_dims
      - .offset:         456
        .size:           4
        .value_kind:     hidden_dynamic_lds_size
    .group_segment_fixed_size: 0
    .kernarg_segment_align: 8
    .kernarg_segment_size: 592
    .language:       OpenCL C
    .language_version:
      - 2
      - 0
    .max_flat_workgroup_size: 512
    .name:           _Z14gemm256_kernelILi1ELi2048ELi512EEv8GemmArgs
    .private_segment_fixed_size: 0
    .sgpr_count:     76
    .sgpr_spill_count: 0
    .symbol:         _Z14gemm256_kernelILi1ELi2048ELi512EEv8GemmArgs.kd
    .uniform_work_group_size: 1
    .uses_dynamic_stack: false
    .vgpr_count:     256
    .vgpr_spill_count: 0
    .wavefront_size: 64
  - .agpr_count:     0
    .args:
      - .offset:         0
        .size:           336
        .value_kind:     by_value
    .group_segment_fixed_size: 0
    .kernarg_segment_align: 8
    .kernarg_segment_size: 336
    .language:       OpenCL C
    .language_version:
      - 2
      - 0
    .max_flat_workgroup_size: 256
    .name:           _Z11gemm_kernelILi4EEv8GemmArgs
    .private_segment_fixed_size: 0
    .sgpr_count:     42
    .sgpr_spill_count: 0
    .symbol:         _Z11gemm_kernelILi4EEv8GemmArgs.kd
    .uniform_work_group_size: 1
    .uses_dynamic_stack: false
    .vgpr_count:     196
    .vgpr_spill_count: 0
    .wavefront_size: 64
  - .agpr_count:     0
    .args:
      - .offset:         0
        .size:           336
        .value_kind:     by_value
    .group_segment_fixed_size: 0
    .kernarg_segment_align: 8
    .kernarg_segment_size: 336
    .language:       OpenCL C
    .language_version:
      - 2
      - 0
    .max_flat_workgroup_size: 256
    .name:           _Z11gemm_kernelILi3EEv8GemmArgs
    .private_segment_fixed_size: 0
    .sgpr_count:     38
    .sgpr_spill_count: 0
    .symbol:         _Z11gemm_kernelILi3EEv8GemmArgs.kd
    .uniform_work_group_size: 1
    .uses_dynamic_stack: false
    .vgpr_count:     200
    .vgpr_spill_count: 0
    .wavefront_size: 64
